# P0 mod partials (silu(c) @ w_ada): 64 f32-operand MFMAs (v_mfma_f32_32x32x2_f32, same k-ordered fma chain, bit-identical) instead of 2048 v_readlane + 2048 v_fmac per wave
# baseline (speedup 1.0000x reference)
; __device__ __forceinline__ float silu_f(float v) { return v * __builtin_amdgcn_rcpf(1.f + __expf(-v)); }
; __device__ __forceinline__ void mod_task(const float* __restrict__ cin, const float* __restrict__ w_ada, float* __restrict__ modp, int task, int lane) {
;     const int cbk = task % 96, kc = task / 96, j = cbk * 64 + lane, k0 = kc * 64;
;     float acc[32], cv[32];
; #pragma unroll
;     for (int b = 0; b < 32; ++b) { acc[b] = 0.f; cv[b] = silu_f(cin[b * D + k0 + lane]); }
; #pragma unroll
;     for (int kb = 0; kb < 4; ++kb) {
;         float w[16];
; #pragma unroll
;         for (int i = 0; i < 16; ++i) w[i] = w_ada[(size_t)(k0 + kb * 16 + i) * 6144 + j];
.LBB0_12:
	s_waitcnt lgkmcnt(0)
	s_mul_hi_i32 s0, s81, 0x2aaaaaab
	s_lshr_b32 s1, s0, 31
	s_ashr_i32 s0, s0, 4
	s_add_i32 s0, s0, s1
	s_mul_i32 s3, s0, 0x60
	s_sub_i32 s3, s81, s3
	s_lshl_b32 s3, s3, 8
	s_lshl_b32 s1, s0, 8
	s_add_u32 s4, s40, s1
	s_addc_u32 s5, s41, 0
	s_mul_i32 s6, s0, 0x180000
	s_add_u32 s6, s6, s3
	s_add_u32 s6, s42, s6
	s_addc_u32 s7, s43, 0
	s_mul_i32 s8, s0, 0xc0000
	s_add_u32 s8, s8, s3
	s_add_u32 s8, s54, s8
	s_addc_u32 s9, s55, 0
	s_lshl_b32 s10, s89, 14
	v_lshlrev_b32_e32 v32, 2, v68
	v_and_b32_e32 v37, 31, v68
	v_lshrrev_b32_e32 v38, 5, v68
	v_mul_u32_u24_e32 v33, 0x6000, v38
	v_lshl_add_u32 v33, v37, 2, v33
	v_mul_u32_u24_e32 v34, 0x18000, v38
	v_lshl_add_u32 v34, v37, 2, v34
	v_add_u32_e32 v35, s10, v32
	v_mul_u32_u24_e32 v36, 0x104, v37
	v_lshl_add_u32 v36, v38, 2, v36
	v_add_u32_e32 v36, s10, v36
	global_load_dword v0, v32, s[4:5]
	s_add_u32 s4, s4, 0x1000
	s_addc_u32 s5, s5, 0
	global_load_dword v1, v32, s[4:5]
	s_add_u32 s4, s4, 0x1000
	s_addc_u32 s5, s5, 0
	global_load_dword v2, v32, s[4:5]
	s_add_u32 s4, s4, 0x1000
	s_addc_u32 s5, s5, 0
	global_load_dword v3, v32, s[4:5]
	s_add_u32 s4, s4, 0x1000
	s_addc_u32 s5, s5, 0
	global_load_dword v4, v32, s[4:5]
	s_add_u32 s4, s4, 0x1000
	s_addc_u32 s5, s5, 0
	global_load_dword v5, v32, s[4:5]
	s_add_u32 s4, s4, 0x1000
	s_addc_u32 s5, s5, 0
	global_load_dword v6, v32, s[4:5]
	s_add_u32 s4, s4, 0x1000
	s_addc_u32 s5, s5, 0
	global_load_dword v7, v32, s[4:5]
	s_add_u32 s4, s4, 0x1000
	s_addc_u32 s5, s5, 0
	global_load_dword v8, v32, s[4:5]
	s_add_u32 s4, s4, 0x1000
	s_addc_u32 s5, s5, 0
	global_load_dword v9, v32, s[4:5]
	s_add_u32 s4, s4, 0x1000
	s_addc_u32 s5, s5, 0
	global_load_dword v10, v32, s[4:5]
	s_add_u32 s4, s4, 0x1000
	s_addc_u32 s5, s5, 0
	global_load_dword v11, v32, s[4:5]
	s_add_u32 s4, s4, 0x1000
	s_addc_u32 s5, s5, 0
	global_load_dword v12, v32, s[4:5]
	s_add_u32 s4, s4, 0x1000
	s_addc_u32 s5, s5, 0
	global_load_dword v13, v32, s[4:5]
	s_add_u32 s4, s4, 0x1000
	s_addc_u32 s5, s5, 0
	global_load_dword v14, v32, s[4:5]
	s_add_u32 s4, s4, 0x1000
	s_addc_u32 s5, s5, 0
	global_load_dword v15, v32, s[4:5]
	s_add_u32 s4, s4, 0x1000
	s_addc_u32 s5, s5, 0
	global_load_dword v16, v32, s[4:5]
	s_add_u32 s4, s4, 0x1000
	s_addc_u32 s5, s5, 0
	global_load_dword v17, v32, s[4:5]
	s_add_u32 s4, s4, 0x1000
	s_addc_u32 s5, s5, 0
	global_load_dword v18, v32, s[4:5]
	s_add_u32 s4, s4, 0x1000
	s_addc_u32 s5, s5, 0
	global_load_dword v19, v32, s[4:5]
	s_add_u32 s4, s4, 0x1000
	s_addc_u32 s5, s5, 0
	global_load_dword v20, v32, s[4:5]
	s_add_u32 s4, s4, 0x1000
	s_addc_u32 s5, s5, 0
	global_load_dword v21, v32, s[4:5]
	s_add_u32 s4, s4, 0x1000
	s_addc_u32 s5, s5, 0
	global_load_dword v22, v32, s[4:5]
	s_add_u32 s4, s4, 0x1000
	s_addc_u32 s5, s5, 0
	global_load_dword v23, v32, s[4:5]
	s_add_u32 s4, s4, 0x1000
	s_addc_u32 s5, s5, 0
	global_load_dword v24, v32, s[4:5]
	s_add_u32 s4, s4, 0x1000
	s_addc_u32 s5, s5, 0
	global_load_dword v25, v32, s[4:5]
	s_add_u32 s4, s4, 0x1000
	s_addc_u32 s5, s5, 0
	global_load_dword v26, v32, s[4:5]
	s_add_u32 s4, s4, 0x1000
	s_addc_u32 s5, s5, 0
	global_load_dword v27, v32, s[4:5]
	s_add_u32 s4, s4, 0x1000
	s_addc_u32 s5, s5, 0
	global_load_dword v28, v32, s[4:5]
	s_add_u32 s4, s4, 0x1000
	s_addc_u32 s5, s5, 0
	global_load_dword v29, v32, s[4:5]
	s_add_u32 s4, s4, 0x1000
	s_addc_u32 s5, s5, 0
	global_load_dword v30, v32, s[4:5]
	s_add_u32 s4, s4, 0x1000
	s_addc_u32 s5, s5, 0
	global_load_dword v31, v32, s[4:5]
	global_load_dword v102, v33, s[6:7]
	global_load_dword v103, v33, s[6:7] offset:128
	s_add_u32 s6, s6, 0xc000
	s_addc_u32 s7, s7, 0
	global_load_dword v104, v33, s[6:7]
	global_load_dword v105, v33, s[6:7] offset:128
	s_add_u32 s6, s6, 0xc000
	s_addc_u32 s7, s7, 0
	global_load_dword v106, v33, s[6:7]
	global_load_dword v107, v33, s[6:7] offset:128
	s_add_u32 s6, s6, 0xc000
	s_addc_u32 s7, s7, 0
	global_load_dword v108, v33, s[6:7]
	global_load_dword v109, v33, s[6:7] offset:128
	s_add_u32 s6, s6, 0xc000
	s_addc_u32 s7, s7, 0
	global_load_dword v110, v33, s[6:7]
	global_load_dword v111, v33, s[6:7] offset:128
	s_add_u32 s6, s6, 0xc000
	s_addc_u32 s7, s7, 0
	global_load_dword v112, v33, s[6:7]
	global_load_dword v113, v33, s[6:7] offset:128
	s_add_u32 s6, s6, 0xc000
	s_addc_u32 s7, s7, 0
	global_load_dword v114, v33, s[6:7]
	global_load_dword v115, v33, s[6:7] offset:128
	s_add_u32 s6, s6, 0xc000
	s_addc_u32 s7, s7, 0
	global_load_dword v116, v33, s[6:7]
	global_load_dword v117, v33, s[6:7] offset:128
	s_add_u32 s6, s6, 0xc000
	s_addc_u32 s7, s7, 0
	global_load_dword v118, v33, s[6:7]
	global_load_dword v119, v33, s[6:7] offset:128
	s_add_u32 s6, s6, 0xc000
	s_addc_u32 s7, s7, 0
	global_load_dword v120, v33, s[6:7]
	global_load_dword v121, v33, s[6:7] offset:128
	s_add_u32 s6, s6, 0xc000
	s_addc_u32 s7, s7, 0
	global_load_dword v122, v33, s[6:7]
	global_load_dword v123, v33, s[6:7] offset:128
	s_add_u32 s6, s6, 0xc000
	s_addc_u32 s7, s7, 0
	global_load_dword v124, v33, s[6:7]
	global_load_dword v125, v33, s[6:7] offset:128
	s_add_u32 s6, s6, 0xc000
	s_addc_u32 s7, s7, 0
	global_load_dword v126, v33, s[6:7]
	global_load_dword v127, v33, s[6:7] offset:128
	s_add_u32 s6, s6, 0xc000
	s_addc_u32 s7, s7, 0
	global_load_dword v128, v33, s[6:7]
	global_load_dword v129, v33, s[6:7] offset:128
	s_add_u32 s6, s6, 0xc000
	s_addc_u32 s7, s7, 0
	global_load_dword v130, v33, s[6:7]
	global_load_dword v131, v33, s[6:7] offset:128
	s_add_u32 s6, s6, 0xc000
	s_addc_u32 s7, s7, 0
	s_waitcnt vmcnt(30)
; __device__ __forceinline__ float silu_f(float v) { return v * __builtin_amdgcn_rcpf(1.f + __expf(-v)); }
; __device__ __forceinline__ void mod_task(const float* __restrict__ cin, const float* __restrict__ w_ada, float* __restrict__ modp, int task, int lane) {
;     ...
;     for (int b = 0; b < 32; ++b) { acc[b] = 0.f; cv[b] = silu_f(cin[b * D + k0 + lane]); }
	v_mul_f32_e32 v40, 0xbfb8aa3b, v0
	v_mul_f32_e32 v41, 0xbfb8aa3b, v1
	v_mul_f32_e32 v42, 0xbfb8aa3b, v2
	v_mul_f32_e32 v43, 0xbfb8aa3b, v3
	v_exp_f32_e32 v40, v40
	v_exp_f32_e32 v41, v41
	v_exp_f32_e32 v42, v42
	v_exp_f32_e32 v43, v43
	s_nop 0
	v_add_f32_e32 v40, 1.0, v40
	v_add_f32_e32 v41, 1.0, v41
	v_add_f32_e32 v42, 1.0, v42
	v_add_f32_e32 v43, 1.0, v43
	v_rcp_f32_e32 v40, v40
	v_rcp_f32_e32 v41, v41
	v_rcp_f32_e32 v42, v42
	v_rcp_f32_e32 v43, v43
	s_nop 0
	v_mul_f32_e32 v0, v0, v40
	v_mul_f32_e32 v1, v1, v41
	v_mul_f32_e32 v2, v2, v42
	v_mul_f32_e32 v3, v3, v43
	v_mul_f32_e32 v40, 0xbfb8aa3b, v4
	v_mul_f32_e32 v41, 0xbfb8aa3b, v5
	v_mul_f32_e32 v42, 0xbfb8aa3b, v6
	v_mul_f32_e32 v43, 0xbfb8aa3b, v7
	v_exp_f32_e32 v40, v40
	v_exp_f32_e32 v41, v41
	v_exp_f32_e32 v42, v42
	v_exp_f32_e32 v43, v43
	s_nop 0
	v_add_f32_e32 v40, 1.0, v40
	v_add_f32_e32 v41, 1.0, v41
	v_add_f32_e32 v42, 1.0, v42
	v_add_f32_e32 v43, 1.0, v43
	v_rcp_f32_e32 v40, v40
	v_rcp_f32_e32 v41, v41
	v_rcp_f32_e32 v42, v42
	v_rcp_f32_e32 v43, v43
	s_nop 0
	v_mul_f32_e32 v4, v4, v40
	v_mul_f32_e32 v5, v5, v41
	v_mul_f32_e32 v6, v6, v42
	v_mul_f32_e32 v7, v7, v43
	v_mul_f32_e32 v40, 0xbfb8aa3b, v8
	v_mul_f32_e32 v41, 0xbfb8aa3b, v9
	v_mul_f32_e32 v42, 0xbfb8aa3b, v10
	v_mul_f32_e32 v43, 0xbfb8aa3b, v11
	v_exp_f32_e32 v40, v40
	v_exp_f32_e32 v41, v41
	v_exp_f32_e32 v42, v42
	v_exp_f32_e32 v43, v43
	s_nop 0
	v_add_f32_e32 v40, 1.0, v40
	v_add_f32_e32 v41, 1.0, v41
	v_add_f32_e32 v42, 1.0, v42
	v_add_f32_e32 v43, 1.0, v43
	v_rcp_f32_e32 v40, v40
	v_rcp_f32_e32 v41, v41
	v_rcp_f32_e32 v42, v42
	v_rcp_f32_e32 v43, v43
	s_nop 0
	v_mul_f32_e32 v8, v8, v40
	v_mul_f32_e32 v9, v9, v41
	v_mul_f32_e32 v10, v10, v42
	v_mul_f32_e32 v11, v11, v43
	v_mul_f32_e32 v40, 0xbfb8aa3b, v12
	v_mul_f32_e32 v41, 0xbfb8aa3b, v13
	v_mul_f32_e32 v42, 0xbfb8aa3b, v14
	v_mul_f32_e32 v43, 0xbfb8aa3b, v15
	v_exp_f32_e32 v40, v40
	v_exp_f32_e32 v41, v41
	v_exp_f32_e32 v42, v42
	v_exp_f32_e32 v43, v43
	s_nop 0
	v_add_f32_e32 v40, 1.0, v40
	v_add_f32_e32 v41, 1.0, v41
	v_add_f32_e32 v42, 1.0, v42
	v_add_f32_e32 v43, 1.0, v43
	v_rcp_f32_e32 v40, v40
	v_rcp_f32_e32 v41, v41
	v_rcp_f32_e32 v42, v42
	v_rcp_f32_e32 v43, v43
	s_nop 0
	v_mul_f32_e32 v12, v12, v40
	v_mul_f32_e32 v13, v13, v41
	v_mul_f32_e32 v14, v14, v42
	v_mul_f32_e32 v15, v15, v43
	v_mul_f32_e32 v40, 0xbfb8aa3b, v16
	v_mul_f32_e32 v41, 0xbfb8aa3b, v17
	v_mul_f32_e32 v42, 0xbfb8aa3b, v18
	v_mul_f32_e32 v43, 0xbfb8aa3b, v19
	v_exp_f32_e32 v40, v40
	v_exp_f32_e32 v41, v41
	v_exp_f32_e32 v42, v42
	v_exp_f32_e32 v43, v43
	s_nop 0
	v_add_f32_e32 v40, 1.0, v40
	v_add_f32_e32 v41, 1.0, v41
	v_add_f32_e32 v42, 1.0, v42
	v_add_f32_e32 v43, 1.0, v43
	v_rcp_f32_e32 v40, v40
	v_rcp_f32_e32 v41, v41
	v_rcp_f32_e32 v42, v42
	v_rcp_f32_e32 v43, v43
	s_nop 0
	v_mul_f32_e32 v16, v16, v40
	v_mul_f32_e32 v17, v17, v41
	v_mul_f32_e32 v18, v18, v42
	v_mul_f32_e32 v19, v19, v43
	v_mul_f32_e32 v40, 0xbfb8aa3b, v20
	v_mul_f32_e32 v41, 0xbfb8aa3b, v21
	v_mul_f32_e32 v42, 0xbfb8aa3b, v22
	v_mul_f32_e32 v43, 0xbfb8aa3b, v23
	v_exp_f32_e32 v40, v40
	v_exp_f32_e32 v41, v41
	v_exp_f32_e32 v42, v42
	v_exp_f32_e32 v43, v43
	s_nop 0
	v_add_f32_e32 v40, 1.0, v40
	v_add_f32_e32 v41, 1.0, v41
	v_add_f32_e32 v42, 1.0, v42
	v_add_f32_e32 v43, 1.0, v43
	v_rcp_f32_e32 v40, v40
	v_rcp_f32_e32 v41, v41
	v_rcp_f32_e32 v42, v42
	v_rcp_f32_e32 v43, v43
	s_nop 0
	v_mul_f32_e32 v20, v20, v40
	v_mul_f32_e32 v21, v21, v41
	v_mul_f32_e32 v22, v22, v42
	v_mul_f32_e32 v23, v23, v43
	v_mul_f32_e32 v40, 0xbfb8aa3b, v24
	v_mul_f32_e32 v41, 0xbfb8aa3b, v25
	v_mul_f32_e32 v42, 0xbfb8aa3b, v26
	v_mul_f32_e32 v43, 0xbfb8aa3b, v27
	v_exp_f32_e32 v40, v40
	v_exp_f32_e32 v41, v41
	v_exp_f32_e32 v42, v42
	v_exp_f32_e32 v43, v43
	s_nop 0
	v_add_f32_e32 v40, 1.0, v40
	v_add_f32_e32 v41, 1.0, v41
	v_add_f32_e32 v42, 1.0, v42
	v_add_f32_e32 v43, 1.0, v43
	v_rcp_f32_e32 v40, v40
	v_rcp_f32_e32 v41, v41
	v_rcp_f32_e32 v42, v42
	v_rcp_f32_e32 v43, v43
	s_nop 0
	v_mul_f32_e32 v24, v24, v40
	v_mul_f32_e32 v25, v25, v41
	v_mul_f32_e32 v26, v26, v42
	v_mul_f32_e32 v27, v27, v43
	v_mul_f32_e32 v40, 0xbfb8aa3b, v28
	v_mul_f32_e32 v41, 0xbfb8aa3b, v29
	v_mul_f32_e32 v42, 0xbfb8aa3b, v30
	v_mul_f32_e32 v43, 0xbfb8aa3b, v31
	v_exp_f32_e32 v40, v40
	v_exp_f32_e32 v41, v41
	v_exp_f32_e32 v42, v42
	v_exp_f32_e32 v43, v43
	s_nop 0
	v_add_f32_e32 v40, 1.0, v40
	v_add_f32_e32 v41, 1.0, v41
	v_add_f32_e32 v42, 1.0, v42
	v_add_f32_e32 v43, 1.0, v43
	v_rcp_f32_e32 v40, v40
	v_rcp_f32_e32 v41, v41
	v_rcp_f32_e32 v42, v42
	v_rcp_f32_e32 v43, v43
	s_nop 0
	v_mul_f32_e32 v28, v28, v40
	v_mul_f32_e32 v29, v29, v41
	v_mul_f32_e32 v30, v30, v42
	v_mul_f32_e32 v31, v31, v43
	ds_write_b32 v35, v0
	ds_write_b32 v35, v1 offset:260
	ds_write_b32 v35, v2 offset:520
	ds_write_b32 v35, v3 offset:780
	ds_write_b32 v35, v4 offset:1040
	ds_write_b32 v35, v5 offset:1300
	ds_write_b32 v35, v6 offset:1560
	ds_write_b32 v35, v7 offset:1820
	ds_write_b32 v35, v8 offset:2080
	ds_write_b32 v35, v9 offset:2340
	ds_write_b32 v35, v10 offset:2600
	ds_write_b32 v35, v11 offset:2860
	ds_write_b32 v35, v12 offset:3120
	ds_write_b32 v35, v13 offset:3380
	ds_write_b32 v35, v14 offset:3640
	ds_write_b32 v35, v15 offset:3900
	ds_write_b32 v35, v16 offset:4160
	ds_write_b32 v35, v17 offset:4420
	ds_write_b32 v35, v18 offset:4680
	ds_write_b32 v35, v19 offset:4940
	ds_write_b32 v35, v20 offset:5200
	ds_write_b32 v35, v21 offset:5460
	ds_write_b32 v35, v22 offset:5720
	ds_write_b32 v35, v23 offset:5980
	ds_write_b32 v35, v24 offset:6240
	ds_write_b32 v35, v25 offset:6500
	ds_write_b32 v35, v26 offset:6760
	ds_write_b32 v35, v27 offset:7020
	ds_write_b32 v35, v28 offset:7280
	ds_write_b32 v35, v29 offset:7540
	ds_write_b32 v35, v30 offset:7800
	ds_write_b32 v35, v31 offset:8060
	s_waitcnt lgkmcnt(0)
; __device__ __forceinline__ void mod_task(const float* __restrict__ cin, const float* __restrict__ w_ada, float* __restrict__ modp, int task, int lane) {
;     ...
;     for (int kb = 0; kb < 4; ++kb) {
;         float w[16];
; #pragma unroll
;         for (int i = 0; i < 16; ++i) w[i] = w_ada[(size_t)(k0 + kb * 16 + i) * 6144 + j];
; #pragma unroll
;         for (int i = 0; i < 16; ++i)
; #pragma unroll
;             for (int b = 0; b < 32; ++b) acc[b] += __builtin_bit_cast(float, __builtin_amdgcn_readlane(__builtin_bit_cast(int, cv[b]), kb * 16 + i)) * w[i];
	ds_read_b32 v70, v36
	ds_read_b32 v71, v36 offset:8
	ds_read_b32 v72, v36 offset:16
	ds_read_b32 v73, v36 offset:24
	ds_read_b32 v74, v36 offset:32
	ds_read_b32 v75, v36 offset:40
	ds_read_b32 v76, v36 offset:48
	ds_read_b32 v77, v36 offset:56
	ds_read_b32 v78, v36 offset:64
	ds_read_b32 v79, v36 offset:72
	ds_read_b32 v80, v36 offset:80
	ds_read_b32 v81, v36 offset:88
	ds_read_b32 v82, v36 offset:96
	ds_read_b32 v83, v36 offset:104
	ds_read_b32 v84, v36 offset:112
	ds_read_b32 v85, v36 offset:120
	ds_read_b32 v86, v36 offset:128
	ds_read_b32 v87, v36 offset:136
	ds_read_b32 v88, v36 offset:144
	ds_read_b32 v89, v36 offset:152
	ds_read_b32 v90, v36 offset:160
	ds_read_b32 v91, v36 offset:168
	ds_read_b32 v92, v36 offset:176
	ds_read_b32 v93, v36 offset:184
	ds_read_b32 v94, v36 offset:192
	ds_read_b32 v95, v36 offset:200
	ds_read_b32 v96, v36 offset:208
	ds_read_b32 v97, v36 offset:216
	ds_read_b32 v98, v36 offset:224
	ds_read_b32 v99, v36 offset:232
	ds_read_b32 v100, v36 offset:240
	ds_read_b32 v101, v36 offset:248
	s_waitcnt vmcnt(16)
	global_load_dword v132, v33, s[6:7]
	global_load_dword v133, v33, s[6:7] offset:128
	s_add_u32 s6, s6, 0xc000
	s_addc_u32 s7, s7, 0
	global_load_dword v134, v33, s[6:7]
	global_load_dword v135, v33, s[6:7] offset:128
	s_add_u32 s6, s6, 0xc000
	s_addc_u32 s7, s7, 0
	global_load_dword v136, v33, s[6:7]
	global_load_dword v137, v33, s[6:7] offset:128
	s_add_u32 s6, s6, 0xc000
	s_addc_u32 s7, s7, 0
	global_load_dword v138, v33, s[6:7]
	global_load_dword v139, v33, s[6:7] offset:128
	s_add_u32 s6, s6, 0xc000
	s_addc_u32 s7, s7, 0
	global_load_dword v140, v33, s[6:7]
	global_load_dword v141, v33, s[6:7] offset:128
	s_add_u32 s6, s6, 0xc000
	s_addc_u32 s7, s7, 0
	global_load_dword v142, v33, s[6:7]
	global_load_dword v143, v33, s[6:7] offset:128
	s_add_u32 s6, s6, 0xc000
	s_addc_u32 s7, s7, 0
	global_load_dword v144, v33, s[6:7]
	global_load_dword v145, v33, s[6:7] offset:128
	s_add_u32 s6, s6, 0xc000
	s_addc_u32 s7, s7, 0
	global_load_dword v146, v33, s[6:7]
	global_load_dword v147, v33, s[6:7] offset:128
	s_add_u32 s6, s6, 0xc000
	s_addc_u32 s7, s7, 0
	global_load_dword v148, v33, s[6:7]
	global_load_dword v149, v33, s[6:7] offset:128
	s_add_u32 s6, s6, 0xc000
	s_addc_u32 s7, s7, 0
	global_load_dword v150, v33, s[6:7]
	global_load_dword v151, v33, s[6:7] offset:128
	s_add_u32 s6, s6, 0xc000
	s_addc_u32 s7, s7, 0
	global_load_dword v152, v33, s[6:7]
	global_load_dword v153, v33, s[6:7] offset:128
	s_add_u32 s6, s6, 0xc000
	s_addc_u32 s7, s7, 0
	global_load_dword v154, v33, s[6:7]
	global_load_dword v155, v33, s[6:7] offset:128
	s_add_u32 s6, s6, 0xc000
	s_addc_u32 s7, s7, 0
	global_load_dword v156, v33, s[6:7]
	global_load_dword v157, v33, s[6:7] offset:128
	s_add_u32 s6, s6, 0xc000
	s_addc_u32 s7, s7, 0
	global_load_dword v158, v33, s[6:7]
	global_load_dword v159, v33, s[6:7] offset:128
	s_add_u32 s6, s6, 0xc000
	s_addc_u32 s7, s7, 0
	global_load_dword v160, v33, s[6:7]
	global_load_dword v161, v33, s[6:7] offset:128
	s_add_u32 s6, s6, 0xc000
	s_addc_u32 s7, s7, 0
	global_load_dword v162, v33, s[6:7]
	global_load_dword v163, v33, s[6:7] offset:128
	s_add_u32 s6, s6, 0xc000
	s_addc_u32 s7, s7, 0
	global_load_dword v164, v33, s[6:7]
	global_load_dword v165, v33, s[6:7] offset:128
	s_waitcnt vmcnt(0) lgkmcnt(0)
; __device__ __forceinline__ void mod_task(const float* __restrict__ cin, const float* __restrict__ w_ada, float* __restrict__ modp, int task, int lane) {
;     ...
;         for (int i = 0; i < 16; ++i)
; #pragma unroll
;             for (int b = 0; b < 32; ++b) acc[b] += __builtin_bit_cast(float, __builtin_amdgcn_readlane(__builtin_bit_cast(int, cv[b]), kb * 16 + i)) * w[i];
;     }
; #pragma unroll
;     for (int b = 0; b < 32; ++b) modp[((size_t)kc * 32 + b) * 6144 + j] = acc[b];
	v_mfma_f32_32x32x2_f32 v[166:181], v70, v102, 0
	v_mfma_f32_32x32x2_f32 v[182:197], v70, v103, 0
	v_mfma_f32_32x32x2_f32 v[166:181], v71, v104, v[166:181]
	v_mfma_f32_32x32x2_f32 v[182:197], v71, v105, v[182:197]
	v_mfma_f32_32x32x2_f32 v[166:181], v72, v106, v[166:181]
	v_mfma_f32_32x32x2_f32 v[182:197], v72, v107, v[182:197]
	v_mfma_f32_32x32x2_f32 v[166:181], v73, v108, v[166:181]
	v_mfma_f32_32x32x2_f32 v[182:197], v73, v109, v[182:197]
	v_mfma_f32_32x32x2_f32 v[166:181], v74, v110, v[166:181]
	v_mfma_f32_32x32x2_f32 v[182:197], v74, v111, v[182:197]
	v_mfma_f32_32x32x2_f32 v[166:181], v75, v112, v[166:181]
	v_mfma_f32_32x32x2_f32 v[182:197], v75, v113, v[182:197]
	v_mfma_f32_32x32x2_f32 v[166:181], v76, v114, v[166:181]
	v_mfma_f32_32x32x2_f32 v[182:197], v76, v115, v[182:197]
	v_mfma_f32_32x32x2_f32 v[166:181], v77, v116, v[166:181]
	v_mfma_f32_32x32x2_f32 v[182:197], v77, v117, v[182:197]
	v_mfma_f32_32x32x2_f32 v[166:181], v78, v118, v[166:181]
	v_mfma_f32_32x32x2_f32 v[182:197], v78, v119, v[182:197]
	v_mfma_f32_32x32x2_f32 v[166:181], v79, v120, v[166:181]
	v_mfma_f32_32x32x2_f32 v[182:197], v79, v121, v[182:197]
	v_mfma_f32_32x32x2_f32 v[166:181], v80, v122, v[166:181]
	v_mfma_f32_32x32x2_f32 v[182:197], v80, v123, v[182:197]
	v_mfma_f32_32x32x2_f32 v[166:181], v81, v124, v[166:181]
	v_mfma_f32_32x32x2_f32 v[182:197], v81, v125, v[182:197]
	v_mfma_f32_32x32x2_f32 v[166:181], v82, v126, v[166:181]
	v_mfma_f32_32x32x2_f32 v[182:197], v82, v127, v[182:197]
	v_mfma_f32_32x32x2_f32 v[166:181], v83, v128, v[166:181]
	v_mfma_f32_32x32x2_f32 v[182:197], v83, v129, v[182:197]
	v_mfma_f32_32x32x2_f32 v[166:181], v84, v130, v[166:181]
	v_mfma_f32_32x32x2_f32 v[182:197], v84, v131, v[182:197]
	v_mfma_f32_32x32x2_f32 v[166:181], v85, v132, v[166:181]
	v_mfma_f32_32x32x2_f32 v[182:197], v85, v133, v[182:197]
	v_mfma_f32_32x32x2_f32 v[166:181], v86, v134, v[166:181]
	v_mfma_f32_32x32x2_f32 v[182:197], v86, v135, v[182:197]
	v_mfma_f32_32x32x2_f32 v[166:181], v87, v136, v[166:181]
	v_mfma_f32_32x32x2_f32 v[182:197], v87, v137, v[182:197]
	v_mfma_f32_32x32x2_f32 v[166:181], v88, v138, v[166:181]
	v_mfma_f32_32x32x2_f32 v[182:197], v88, v139, v[182:197]
	v_mfma_f32_32x32x2_f32 v[166:181], v89, v140, v[166:181]
	v_mfma_f32_32x32x2_f32 v[182:197], v89, v141, v[182:197]
	v_mfma_f32_32x32x2_f32 v[166:181], v90, v142, v[166:181]
	v_mfma_f32_32x32x2_f32 v[182:197], v90, v143, v[182:197]
	v_mfma_f32_32x32x2_f32 v[166:181], v91, v144, v[166:181]
	v_mfma_f32_32x32x2_f32 v[182:197], v91, v145, v[182:197]
	v_mfma_f32_32x32x2_f32 v[166:181], v92, v146, v[166:181]
	v_mfma_f32_32x32x2_f32 v[182:197], v92, v147, v[182:197]
	v_mfma_f32_32x32x2_f32 v[166:181], v93, v148, v[166:181]
	v_mfma_f32_32x32x2_f32 v[182:197], v93, v149, v[182:197]
	v_mfma_f32_32x32x2_f32 v[166:181], v94, v150, v[166:181]
	v_mfma_f32_32x32x2_f32 v[182:197], v94, v151, v[182:197]
	v_mfma_f32_32x32x2_f32 v[166:181], v95, v152, v[166:181]
	v_mfma_f32_32x32x2_f32 v[182:197], v95, v153, v[182:197]
	v_mfma_f32_32x32x2_f32 v[166:181], v96, v154, v[166:181]
	v_mfma_f32_32x32x2_f32 v[182:197], v96, v155, v[182:197]
	v_mfma_f32_32x32x2_f32 v[166:181], v97, v156, v[166:181]
	v_mfma_f32_32x32x2_f32 v[182:197], v97, v157, v[182:197]
	v_mfma_f32_32x32x2_f32 v[166:181], v98, v158, v[166:181]
	v_mfma_f32_32x32x2_f32 v[182:197], v98, v159, v[182:197]
	v_mfma_f32_32x32x2_f32 v[166:181], v99, v160, v[166:181]
	v_mfma_f32_32x32x2_f32 v[182:197], v99, v161, v[182:197]
	v_mfma_f32_32x32x2_f32 v[166:181], v100, v162, v[166:181]
	v_mfma_f32_32x32x2_f32 v[182:197], v100, v163, v[182:197]
	v_mfma_f32_32x32x2_f32 v[166:181], v101, v164, v[166:181]
	v_mfma_f32_32x32x2_f32 v[182:197], v101, v165, v[182:197]
	s_nop 15
	s_nop 7
	s_mov_b64 s[12:13], s[8:9]
	global_store_dword v34, v166, s[12:13]
	global_store_dword v34, v182, s[12:13] offset:128
	s_add_u32 s12, s8, 0x6000
	s_addc_u32 s13, s9, 0
	global_store_dword v34, v167, s[12:13]
	global_store_dword v34, v183, s[12:13] offset:128
	s_add_u32 s12, s8, 0xc000
	s_addc_u32 s13, s9, 0
	global_store_dword v34, v168, s[12:13]
	global_store_dword v34, v184, s[12:13] offset:128
	s_add_u32 s12, s8, 0x12000
	s_addc_u32 s13, s9, 0
	global_store_dword v34, v169, s[12:13]
	global_store_dword v34, v185, s[12:13] offset:128
	s_add_u32 s12, s8, 0x30000
	s_addc_u32 s13, s9, 0
	global_store_dword v34, v170, s[12:13]
	global_store_dword v34, v186, s[12:13] offset:128
	s_add_u32 s12, s8, 0x36000
	s_addc_u32 s13, s9, 0
	global_store_dword v34, v171, s[12:13]
	global_store_dword v34, v187, s[12:13] offset:128
	s_add_u32 s12, s8, 0x3c000
	s_addc_u32 s13, s9, 0
	global_store_dword v34, v172, s[12:13]
	global_store_dword v34, v188, s[12:13] offset:128
	s_add_u32 s12, s8, 0x42000
	s_addc_u32 s13, s9, 0
	global_store_dword v34, v173, s[12:13]
	global_store_dword v34, v189, s[12:13] offset:128
	s_add_u32 s12, s8, 0x60000
	s_addc_u32 s13, s9, 0
	global_store_dword v34, v174, s[12:13]
	global_store_dword v34, v190, s[12:13] offset:128
	s_add_u32 s12, s8, 0x66000
	s_addc_u32 s13, s9, 0
	global_store_dword v34, v175, s[12:13]
	global_store_dword v34, v191, s[12:13] offset:128
	s_add_u32 s12, s8, 0x6c000
	s_addc_u32 s13, s9, 0
	global_store_dword v34, v176, s[12:13]
	global_store_dword v34, v192, s[12:13] offset:128
	s_add_u32 s12, s8, 0x72000
	s_addc_u32 s13, s9, 0
	global_store_dword v34, v177, s[12:13]
	global_store_dword v34, v193, s[12:13] offset:128
	s_add_u32 s12, s8, 0x90000
	s_addc_u32 s13, s9, 0
	global_store_dword v34, v178, s[12:13]
	global_store_dword v34, v194, s[12:13] offset:128
	s_add_u32 s12, s8, 0x96000
	s_addc_u32 s13, s9, 0
	global_store_dword v34, v179, s[12:13]
	global_store_dword v34, v195, s[12:13] offset:128
	s_add_u32 s12, s8, 0x9c000
	s_addc_u32 s13, s9, 0
	global_store_dword v34, v180, s[12:13]
	global_store_dword v34, v196, s[12:13] offset:128
	s_add_u32 s12, s8, 0xa2000
	s_addc_u32 s13, s9, 0
	global_store_dword v34, v181, s[12:13]
	global_store_dword v34, v197, s[12:13] offset:128
	s_waitcnt vmcnt(0)
	s_add_i32 s81, s81, s57
	s_cmpk_lt_i32 s81, 0x600
	s_cbranch_scc1 .LBB0_12
